# softmax hand-rewrite v3 (strided partial loads first, interleaved max/sum reductions, tree sums); prep and stream as v35
# speedup vs baseline: 1.0131x; 1.0131x over previous
_Z14softmax_kernelPKfPf:
	s_load_dwordx4 s[4:7], s[0:1], 0x0
	v_and_b32_e32 v1, 63, v0
	v_lshlrev_b32_e32 v2, 4, v0
	v_add_u32_e32 v3, 0x1000, v2
	s_lshl_b32 s8, s2, 13
	s_add_i32 s9, s8, 0x6040
	s_lshl_b32 s10, s2, 2
	s_add_i32 s10, s10, 0x4000
	v_lshl_add_u32 v16, v1, 6, s10
	v_add_u32_e32 v17, 0x1000, v16
	v_lshrrev_b32_e32 v20, 6, v0
	v_lshlrev_b32_e32 v20, 2, v20
	v_mov_b32_e32 v21, 0
	s_waitcnt lgkmcnt(0)
	global_load_dword v12, v16, s[4:5]
	global_load_dword v13, v17, s[4:5]
	s_add_u32 s12, s4, s9
	s_addc_u32 s13, s5, 0
	global_load_dwordx4 v[4:7], v2, s[12:13]
	global_load_dwordx4 v[8:11], v3, s[12:13]
	s_load_dword s16, s[4:5], 0x6000
	s_add_u32 s14, s6, s8
	s_addc_u32 s15, s7, 0
	v_cmp_eq_u32_e32 vcc, 0, v1
	s_waitcnt vmcnt(2)
	v_add_f32_e32 v12, v12, v13
	s_waitcnt vmcnt(0)
	v_max3_f32 v14, v4, v5, v6
	v_max3_f32 v15, v7, v8, v9
	v_max3_f32 v14, v14, v10, v11
	s_nop 0
	v_max_f32_e32 v14, v14, v15
	s_nop 1
	v_max_f32_dpp v14, v14, v14 quad_perm:[1,0,3,2] row_mask:0xf bank_mask:0xf bound_ctrl:1
	s_nop 0
	v_add_f32_dpp v12, v12, v12 quad_perm:[1,0,3,2] row_mask:0xf bank_mask:0xf bound_ctrl:1
	s_nop 0
	v_max_f32_dpp v14, v14, v14 quad_perm:[2,3,0,1] row_mask:0xf bank_mask:0xf bound_ctrl:1
	s_nop 0
	v_add_f32_dpp v12, v12, v12 quad_perm:[2,3,0,1] row_mask:0xf bank_mask:0xf bound_ctrl:1
	s_nop 0
	v_max_f32_dpp v14, v14, v14 row_ror:4 row_mask:0xf bank_mask:0xf bound_ctrl:1
	s_nop 0
	v_add_f32_dpp v12, v12, v12 row_ror:4 row_mask:0xf bank_mask:0xf bound_ctrl:1
	s_nop 0
	v_max_f32_dpp v14, v14, v14 row_ror:8 row_mask:0xf bank_mask:0xf bound_ctrl:1
	s_nop 0
	v_add_f32_dpp v12, v12, v12 row_ror:8 row_mask:0xf bank_mask:0xf bound_ctrl:1
	v_mov_b32_e32 v15, v14
	v_mov_b32_e32 v13, v12
	s_nop 1
	v_permlane16_swap_b32_e32 v14, v15
	v_permlane16_swap_b32_e32 v12, v13
	v_max_f32_e32 v14, v14, v15
	v_add_f32_e32 v12, v12, v13
	v_mov_b32_e32 v15, v14
	v_mov_b32_e32 v13, v12
	s_nop 1
	v_permlane32_swap_b32_e32 v14, v15
	v_permlane32_swap_b32_e32 v12, v13
	v_max_f32_e32 v14, v14, v15
	v_add_f32_e32 v12, v12, v13
	s_and_saveexec_b64 s[18:19], vcc
	ds_write_b32 v20, v14
	s_mov_b64 exec, s[18:19]
	s_waitcnt lgkmcnt(0)
	s_barrier
	ds_read_b128 v[22:25], v21
	v_add_f32_e32 v12, s16, v12
	v_pk_add_f32 v[4:5], v[4:5], v[12:13] op_sel_hi:[1,0]
	v_pk_add_f32 v[6:7], v[6:7], v[12:13] op_sel_hi:[1,0]
	v_pk_add_f32 v[8:9], v[8:9], v[12:13] op_sel_hi:[1,0]
	v_pk_add_f32 v[10:11], v[10:11], v[12:13] op_sel_hi:[1,0]
	s_waitcnt lgkmcnt(0)
	v_max_f32_e32 v22, v22, v23
	v_max3_f32 v22, v22, v24, v25
	v_add_f32_e32 v22, v22, v12
	v_sub_f32_e32 v4, v4, v22
	v_sub_f32_e32 v5, v5, v22
	v_sub_f32_e32 v6, v6, v22
	v_sub_f32_e32 v7, v7, v22
	v_sub_f32_e32 v8, v8, v22
	v_sub_f32_e32 v9, v9, v22
	v_sub_f32_e32 v10, v10, v22
	v_sub_f32_e32 v11, v11, v22
	v_mul_f32_e32 v4, 0x3fb8aa3b, v4
	v_mul_f32_e32 v5, 0x3fb8aa3b, v5
	v_mul_f32_e32 v6, 0x3fb8aa3b, v6
	v_mul_f32_e32 v7, 0x3fb8aa3b, v7
	v_mul_f32_e32 v8, 0x3fb8aa3b, v8
	v_mul_f32_e32 v9, 0x3fb8aa3b, v9
	v_mul_f32_e32 v10, 0x3fb8aa3b, v10
	v_mul_f32_e32 v11, 0x3fb8aa3b, v11
	v_exp_f32_e32 v4, v4
	v_exp_f32_e32 v5, v5
	v_exp_f32_e32 v6, v6
	v_exp_f32_e32 v7, v7
	v_exp_f32_e32 v8, v8
	v_exp_f32_e32 v9, v9
	v_exp_f32_e32 v10, v10
	v_exp_f32_e32 v11, v11
	v_add_f32_e32 v26, v4, v5
	v_add_f32_e32 v27, v6, v7
	v_add_f32_e32 v28, v8, v9
	s_nop 0
	v_add_f32_e32 v29, v10, v11
	v_add_f32_e32 v26, v26, v27
	v_add_f32_e32 v28, v28, v29
	v_add_f32_e32 v26, v26, v28
	s_nop 1
	v_add_f32_dpp v26, v26, v26 quad_perm:[1,0,3,2] row_mask:0xf bank_mask:0xf bound_ctrl:1
	s_nop 1
	v_add_f32_dpp v26, v26, v26 quad_perm:[2,3,0,1] row_mask:0xf bank_mask:0xf bound_ctrl:1
	s_nop 1
	v_add_f32_dpp v26, v26, v26 row_ror:4 row_mask:0xf bank_mask:0xf bound_ctrl:1
	s_nop 1
	v_add_f32_dpp v26, v26, v26 row_ror:8 row_mask:0xf bank_mask:0xf bound_ctrl:1
	v_mov_b32_e32 v27, v26
	s_nop 1
	v_permlane16_swap_b32_e32 v26, v27
	v_add_f32_e32 v26, v26, v27
	v_mov_b32_e32 v27, v26
	s_nop 1
	v_permlane32_swap_b32_e32 v26, v27
	v_add_f32_e32 v26, v26, v27
	s_and_saveexec_b64 s[18:19], vcc
	ds_write_b32 v20, v26 offset:16
	s_mov_b64 exec, s[18:19]
	s_waitcnt lgkmcnt(0)
	s_barrier
	ds_read_b128 v[22:25], v21 offset:16
	s_waitcnt lgkmcnt(0)
	v_add_f32_e32 v22, v22, v23
	v_add_f32_e32 v24, v24, v25
	v_add_f32_e32 v22, v22, v24
	v_div_scale_f32 v23, s[2:3], v22, v22, 1.0
	v_rcp_f32_e32 v24, v23
	v_div_scale_f32 v25, vcc, 1.0, v22, 1.0
	v_fma_f32 v26, -v23, v24, 1.0
	v_fmac_f32_e32 v24, v26, v24
	v_mul_f32_e32 v26, v25, v24
	v_fma_f32 v27, -v23, v26, v25
	v_fmac_f32_e32 v26, v27, v24
	v_fma_f32 v23, -v23, v26, v25
	v_div_fmas_f32 v23, v23, v24, v26
	v_div_fixup_f32 v26, v23, v22, 1.0
	v_pk_mul_f32 v[4:5], v[4:5], v[26:27] op_sel_hi:[1,0]
	v_pk_mul_f32 v[6:7], v[6:7], v[26:27] op_sel_hi:[1,0]
	v_pk_mul_f32 v[8:9], v[8:9], v[26:27] op_sel_hi:[1,0]
	v_pk_mul_f32 v[10:11], v[10:11], v[26:27] op_sel_hi:[1,0]
	global_store_dwordx4 v2, v[4:7], s[14:15]
	global_store_dwordx4 v3, v[8:11], s[14:15]
	s_endpgm

amdhsa.kernels:
  - .agpr_count:     0
    .args:
      - .actual_access:  read_only
        .address_space:  global
        .offset:         0
        .size:           8
        .value_kind:     global_buffer
      - .actual_access:  read_only
        .address_space:  global
        .offset:         8
        .size:           8
        .value_kind:     global_buffer
      - .actual_access:  read_only
        .address_space:  global
        .offset:         16
        .size:           8
        .value_kind:     global_buffer
      - .actual_access:  read_only
        .address_space:  global
        .offset:         24
        .size:           8
        .value_kind:     global_buffer
      - .actual_access:  write_only
        .address_space:  global
        .offset:         32
        .size:           8
        .value_kind:     global_buffer
    .group_segment_fixed_size: 2112
    .kernarg_segment_align: 8
    .kernarg_segment_size: 40
    .language:       OpenCL C
    .language_version:
      - 2
      - 0
    .max_flat_workgroup_size: 1024
    .name:           _Z11prep_kernelPKfS0_S0_S0_Pf
    .private_segment_fixed_size: 0
    .sgpr_count:     34
    .sgpr_spill_count: 0
    .symbol:         _Z11prep_kernelPKfS0_S0_S0_Pf.kd
    .uniform_work_group_size: 1
    .uses_dynamic_stack: false
    .vgpr_count:     72
    .vgpr_spill_count: 0
    .wavefront_size: 64
  - .agpr_count:     0
    .args:
      - .actual_access:  read_only
        .address_space:  global
        .offset:         0
        .size:           8
        .value_kind:     global_buffer
      - .address_space:  global
        .offset:         8
        .size:           8
        .value_kind:     global_buffer
    .group_segment_fixed_size: 4096
    .kernarg_segment_align: 8
    .kernarg_segment_size: 16
    .language:       OpenCL C
    .language_version:
      - 2
      - 0
    .max_flat_workgroup_size: 1024
    .name:           _Z13stream_kernelPKfPf
    .private_segment_fixed_size: 0
    .sgpr_count:     17
    .sgpr_spill_count: 0
    .symbol:         _Z13stream_kernelPKfPf.kd
    .uniform_work_group_size: 1
    .uses_dynamic_stack: false
    .vgpr_count:     67
    .vgpr_spill_count: 0
    .wavefront_size: 64
  - .agpr_count:     0
    .args:
      - .actual_access:  read_only
        .address_space:  global
        .offset:         0
        .size:           8
        .value_kind:     global_buffer
      - .actual_access:  write_only
        .address_space:  global
        .offset:         8
        .size:           8
        .value_kind:     global_buffer
    .group_segment_fixed_size: 32
    .kernarg_segment_align: 8
    .kernarg_segment_size: 16
    .language:       OpenCL C
    .language_version:
      - 2
      - 0
    .max_flat_workgroup_size: 256
    .name:           _Z14softmax_kernelPKfPf
    .private_segment_fixed_size: 0
    .sgpr_count:     26
    .sgpr_spill_count: 0
    .symbol:         _Z14softmax_kernelPKfPf.kd
    .uniform_work_group_size: 1
    .uses_dynamic_stack: false
    .vgpr_count:     32
    .vgpr_spill_count: 0
    .wavefront_size: 64
